# code placement: P8 K-loop +16 bytes, P9 and later code at the same address modulo 64 as the best version
# speedup vs baseline: 1.0022x; 1.0002x over previous
.LBB0_1167:
	s_nop 0
	s_nop 0
	s_nop 0
	s_nop 0
	v_readlane_b32 s2, v251, 14
	v_readlane_b32 s3, v251, 15
	s_cmp_lt_i32 s2, 9
	s_cselect_b64 s[2:3], -1, 0
	s_and_b64 s[0:1], s[2:3], s[0:1]
	s_andn2_b64 vcc, exec, s[0:1]
	s_cbranch_vccnz .LBB0_1200
	v_readlane_b32 s0, v251, 16
	v_mbcnt_lo_u32_b32 v0, -1, 0
	v_mbcnt_hi_u32_b32 v0, -1, v0
	s_andn2_b32 s0, s0, 63
	s_nop 0
	v_add_u32_e32 v0, s0, v0
	v_cmp_gt_i32_e32 vcc, 33, v0
	s_waitcnt lgkmcnt(0)
	v_lshl_add_u32 v2, v0, 2, 0
	s_and_saveexec_b64 s[4:5], vcc
	s_cbranch_execz .LBB0_1170
	v_readlane_b32 s8, v251, 10
	v_ashrrev_i32_e32 v1, 31, v0
	v_readlane_b32 s10, v251, 12
	v_readlane_b32 s11, v251, 13
	v_add_u32_e32 v3, 0x24240, v2
	v_readlane_b32 s9, v251, 11
	v_lshl_add_u64 v[4:5], v[0:1], 2, s[10:11]
	v_add_co_u32_e32 v4, vcc, 0x66280000, v4
	s_nop 1
	v_addc_co_u32_e32 v5, vcc, 0, v5, vcc
	global_load_dword v1, v[4:5], off
	s_waitcnt vmcnt(0)
	ds_write_b32 v3, v1

.LBB0_1252:
	s_nop 0
	s_nop 0
	s_nop 0
	s_nop 0
	s_nop 0
	s_nop 0
	s_nop 0
	s_nop 0
	s_nop 0
	s_nop 0
	s_nop 0
	s_nop 0
	v_readlane_b32 s2, v251, 14
	v_readlane_b32 s3, v251, 15
	s_cmp_lt_i32 s2, 10
	s_cselect_b64 s[2:3], -1, 0
	s_and_b64 s[0:1], s[2:3], s[0:1]
	s_andn2_b64 vcc, exec, s[0:1]
	s_cbranch_vccnz .LBB0_1293
	v_readlane_b32 s0, v251, 16
	v_mbcnt_lo_u32_b32 v0, -1, 0
	v_mbcnt_hi_u32_b32 v0, -1, v0
	s_and_b32 s6, s0, 0xffffffc0
	v_add_u32_e32 v0, s6, v0
	v_cmp_gt_i32_e32 vcc, 33, v0
	s_waitcnt lgkmcnt(0)
	v_lshl_add_u32 v2, v0, 2, 0
	s_and_saveexec_b64 s[0:1], vcc
	s_cbranch_execz .LBB0_1255
	v_readlane_b32 s8, v251, 10
	v_ashrrev_i32_e32 v1, 31, v0
	v_readlane_b32 s10, v251, 12
	v_readlane_b32 s11, v251, 13
	v_add_u32_e32 v3, 0x24240, v2
	v_readlane_b32 s9, v251, 11
	v_lshl_add_u64 v[4:5], v[0:1], 2, s[10:11]
	v_add_co_u32_e32 v4, vcc, 0x66280000, v4
	s_nop 1
	v_addc_co_u32_e32 v5, vcc, 0, v5, vcc
	global_load_dword v1, v[4:5], off
	s_waitcnt vmcnt(0)
	ds_write_b32 v3, v1
